# DSA top-k: threshold-bin candidates chosen by 256-way sub-bin histogram + exact tie list instead of O(C^2) ranking (same selected set)
# speedup vs baseline: 1.0241x; 1.0241x over previous
.LBB0_964:
	s_or_b64 exec, exec, s[2:3]
	v_mov_b32_e32 v132, 0
	v_mov_b32_e32 v133, 0
	v_mov_b32_e32 v134, 0
	v_mov_b32_e32 v135, 0
	ds_write_b128 v235, v[132:135]
	ds_write_b128 v235, v[132:135] offset:16
	s_add_i32 s75, s75, 1
	s_lshl_b32 s2, s75, 3
	s_add_i32 s2, s2, 63
	s_lshl_b32 s60, s75, 4
	s_and_b32 s2, s2, 0x7fffffc0
	v_mov_b32_e32 v4, s2
	v_mov_b32_e32 v5, s60
	v_cndmask_b32_e64 v128, v4, 0, s[8:9]
	v_cndmask_b32_e64 v129, v5, v4, s[8:9]
	s_waitcnt lgkmcnt(0)
	s_barrier
	ds_read2_b32 v[122:123], v165 offset1:4
	v_sub_u32_e32 v4, v129, v128
	v_add_u32_e32 v4, 63, v4
	v_mov_b32_e32 v118, 0
	v_ashrrev_i32_e32 v130, 6, v4
	v_cmp_lt_i32_e32 vcc, 0, v130
	v_mov_b32_e32 v119, v118
	v_mov_b32_e32 v4, v118
	v_mov_b32_e32 v5, v118
	s_and_saveexec_b64 s[2:3], vcc
	s_cbranch_execz .LBB0_970
	v_add_u32_e32 v131, v158, v128
	v_mov_b32_e32 v118, 0
	v_lshl_add_u32 v132, v131, 2, v170
	v_mov_b32_e32 v119, v118
	v_mov_b32_e32 v4, v118
	v_mov_b32_e32 v5, v118
	v_readfirstlane_b32 s99, v130
	s_mov_b32 m0, 0
	ds_read_b32 v134, v132

.LBB0_976:
	v_cmp_gt_u32_e32 vcc, s82, v118
	s_and_saveexec_b64 s[38:39], vcc
	s_cbranch_execz .LBB0_975
	v_ffbl_b32_e32 v129, v5
	v_add_u32_e32 v129, 32, v129
	v_ffbl_b32_e32 v130, v4
	v_min_u32_e32 v129, v130, v129
	v_or_b32_e32 v129, v128, v129
	v_lshl_add_u32 v130, v129, 2, v170
	ds_read_b32 v130, v130
	v_add_u32_e32 v131, 0x1ff, v119
	v_cndmask_b32_e64 v131, v131, v118, s[8:9]
	v_or_b32_e32 v131, v131, v163
	v_lshl_add_u32 v132, v131, 2, 0
	s_waitcnt lgkmcnt(0)
	v_lshlrev_b32_e32 v130, 10, v130
	v_and_b32_e32 v130, 0x7ffffc00, v130
	v_add3_u32 v130, v172, v119, v130
	v_add_u32_e32 v132, 0x24a00, v132
	ds_write_b32 v132, v130
	v_lshrrev_b32_e32 v132, 23, v130
	v_lshl_add_u32 v132, v132, 2, v166
	v_mov_b32_e32 v133, 1
	ds_add_u32 v132, v133
	v_lshl_add_u32 v130, v131, 1, 0
	v_add_u32_e32 v130, 0x26a00, v130
	ds_write_b16 v130, v129
	s_branch .LBB0_975

.LBB0_1014:
	ds_read_b64 v[124:125], v173 offset:48
	v_mov_b32_e32 v129, -1
	s_waitcnt lgkmcnt(0)
	v_add_u32_e32 v3, v125, v124
	v_sub_u32_e32 v4, v216, v3
	v_cmp_lt_i32_e64 s[36:37], v162, v124
	v_cmp_lt_i32_e32 vcc, v162, v3
	s_nop 0
	v_cndmask_b32_e64 v4, v4, v162, s[36:37]
	s_and_saveexec_b64 s[2:3], vcc
	v_lshl_add_u32 v5, v4, 2, v175
	ds_read_b32 v129, v5
	s_or_b64 exec, exec, s[2:3]
	v_mov_b32_e32 v122, 0
	s_and_saveexec_b64 s[2:3], vcc
	v_lshl_add_u32 v4, v4, 1, v176
	ds_read_u16 v122, v4
	s_or_b64 exec, exec, s[2:3]
	v_sub_u32_e32 v4, v217, v3
	v_cmp_lt_i32_e64 s[36:37], v213, v124
	v_mov_b32_e32 v130, -1
	s_nop 0
	v_cndmask_b32_e64 v4, v4, v213, s[36:37]
	v_cmp_lt_i32_e64 s[36:37], v213, v3
	s_and_saveexec_b64 s[2:3], s[36:37]
	v_lshl_add_u32 v5, v4, 2, v175
	ds_read_b32 v130, v5
	s_or_b64 exec, exec, s[2:3]
	v_mov_b32_e32 v126, 0
	s_and_saveexec_b64 s[2:3], s[36:37]
	v_lshl_add_u32 v4, v4, 1, v176
	ds_read_u16 v126, v4
	s_or_b64 exec, exec, s[2:3]
	v_sub_u32_e32 v4, v218, v3
	v_cmp_lt_i32_e64 s[38:39], v214, v124
	v_mov_b32_e32 v5, -1
	s_nop 0
	v_cndmask_b32_e64 v4, v4, v214, s[38:39]
	v_cmp_lt_i32_e64 s[38:39], v214, v3
	s_and_saveexec_b64 s[2:3], s[38:39]
	v_lshl_add_u32 v5, v4, 2, v175
	ds_read_b32 v5, v5
	s_or_b64 exec, exec, s[2:3]
	v_mov_b32_e32 v127, 0
	s_and_saveexec_b64 s[2:3], s[38:39]
	v_lshl_add_u32 v4, v4, 1, v176
	ds_read_u16 v127, v4
	s_or_b64 exec, exec, s[2:3]
	v_sub_u32_e32 v4, v219, v3
	v_cmp_lt_i32_e64 s[40:41], v215, v124
	v_mov_b32_e32 v120, -1
	s_nop 0
	v_cndmask_b32_e64 v4, v4, v215, s[40:41]
	v_cmp_lt_i32_e64 s[40:41], v215, v3
	s_and_saveexec_b64 s[2:3], s[40:41]
	v_lshl_add_u32 v118, v4, 2, v175
	ds_read_b32 v120, v118
	s_or_b64 exec, exec, s[2:3]
	v_mov_b32_e32 v128, 0
	s_and_saveexec_b64 s[2:3], s[40:41]
	v_lshl_add_u32 v4, v4, 1, v176
	ds_read_u16 v128, v4
	s_or_b64 exec, exec, s[2:3]
	s_mov_b64 s[42:43], vcc
	v_lshl_add_u32 v131, v158, 4, v166
	ds_read_b128 v[132:135], v131
	v_sub_u32_e32 v140, v231, v123
	v_lshl_add_u32 v140, v140, 1, v164
	v_add_lshl_u32 v136, v158, 1, 2
	s_waitcnt lgkmcnt(0)
	v_add_u32_e32 v118, v132, v133
	v_add3_u32 v118, v118, v134, v135
	s_nop 0
	ds_bpermute_b32 v137, v136, v118
	v_add_lshl_u32 v136, v158, 2, 2
	s_waitcnt lgkmcnt(0)
	v_cndmask_b32_e64 v137, v137, 0, s[14:15]
	v_add_u32_e32 v119, v118, v137
	ds_bpermute_b32 v137, v136, v119
	v_add_lshl_u32 v136, v158, 4, 2
	s_waitcnt lgkmcnt(0)
	v_cndmask_b32_e64 v137, 0, v137, s[16:17]
	v_add_u32_e32 v119, v119, v137
	ds_bpermute_b32 v137, v136, v119
	v_add_lshl_u32 v136, v158, 8, 2
	s_waitcnt lgkmcnt(0)
	v_cndmask_b32_e64 v137, 0, v137, s[18:19]
	v_add_u32_e32 v119, v119, v137
	ds_bpermute_b32 v137, v136, v119
	v_add_lshl_u32 v136, v158, 16, 2
	s_waitcnt lgkmcnt(0)
	v_cndmask_b32_e64 v137, 0, v137, s[20:21]
	v_add_u32_e32 v119, v119, v137
	ds_bpermute_b32 v137, v136, v119
	v_add_lshl_u32 v136, v158, 32, 2
	s_waitcnt lgkmcnt(0)
	v_cndmask_b32_e64 v137, 0, v137, s[22:23]
	v_add_u32_e32 v119, v119, v137
	ds_bpermute_b32 v137, v136, v119
	s_waitcnt lgkmcnt(0)
	v_cndmask_b32_e64 v137, 0, v137, s[24:25]
	v_add_u32_e32 v119, v119, v137
	v_sub_u32_e32 v121, v119, v118
	v_add_u32_e32 v138, v121, v135
	v_add_u32_e32 v139, v138, v134
	v_add_u32_e32 v141, v139, v133
	v_cmp_lt_i32_e32 vcc, v121, v123
	v_cmp_le_i32_e64 s[44:45], v123, v119
	s_and_b64 s[44:45], vcc, s[44:45]
	v_cmp_ge_i32_e32 vcc, v141, v123
	s_nop 1
	v_cndmask_b32_e32 v136, v141, v139, vcc
	v_cndmask_b32_e32 v137, v132, v133, vcc
	v_cndmask_b32_e64 v141, 0, 1, vcc
	v_cmp_ge_i32_e32 vcc, v139, v123
	s_nop 1
	v_cndmask_b32_e32 v136, v136, v138, vcc
	v_cndmask_b32_e32 v137, v137, v134, vcc
	v_cndmask_b32_e64 v141, v141, 2, vcc
	v_cmp_ge_i32_e32 vcc, v138, v123
	s_nop 1
	v_cndmask_b32_e32 v136, v136, v121, vcc
	v_cndmask_b32_e32 v137, v137, v135, vcc
	v_cndmask_b32_e64 v141, v141, 3, vcc
	s_ff1_i32_b64 s60, s[44:45]
	s_nop 1
	v_readlane_b32 s61, v136, s60
	v_readlane_b32 s62, v137, s60
	v_readlane_b32 s63, v141, s60
	s_lshl_b32 s60, s60, 2
	s_nop 1
	s_add_i32 s63, s63, s60
	s_add_i32 s66, s61, -1
	s_and_b64 s[2:3], s[8:9], exec
	s_cselect_b32 s65, 1, -1
	s_cselect_b32 s66, 0, s66
	v_mov_b32_e32 v138, s65
	v_mov_b32_e32 v139, s66
	s_mov_b32 s64, 0
	v_lshrrev_b32_e32 v131, 23, v129
	v_lshrrev_b32_e32 v132, 23, v130
	v_lshrrev_b32_e32 v133, 23, v5
	v_lshrrev_b32_e32 v134, 23, v120
	v_cmp_lt_u32_e32 vcc, s63, v131
	v_cmp_eq_u32_e64 s[2:3], s63, v131
	s_and_b64 s[44:45], vcc, s[42:43]
	s_and_b64 s[42:43], s[2:3], s[42:43]
	v_mbcnt_lo_u32_b32 v135, s44, 0
	v_mbcnt_hi_u32_b32 v135, s45, v135
	v_add_u32_e32 v135, s64, v135
	v_mad_i32_i24 v135, v135, v138, v139
	v_lshl_add_u32 v135, v135, 1, v140
	s_and_saveexec_b64 s[2:3], s[44:45]
	ds_write_b16 v135, v122
	s_mov_b64 exec, s[2:3]
	s_bcnt1_i32_b64 s60, s[44:45]
	s_add_i32 s64, s64, s60
	v_cmp_lt_u32_e32 vcc, s63, v132
	v_cmp_eq_u32_e64 s[2:3], s63, v132
	s_and_b64 s[44:45], vcc, s[36:37]
	s_and_b64 s[36:37], s[2:3], s[36:37]
	v_mbcnt_lo_u32_b32 v135, s44, 0
	v_mbcnt_hi_u32_b32 v135, s45, v135
	v_add_u32_e32 v135, s64, v135
	v_mad_i32_i24 v135, v135, v138, v139
	v_lshl_add_u32 v135, v135, 1, v140
	s_and_saveexec_b64 s[2:3], s[44:45]
	ds_write_b16 v135, v126
	s_mov_b64 exec, s[2:3]
	s_bcnt1_i32_b64 s60, s[44:45]
	s_add_i32 s64, s64, s60
	v_cmp_lt_u32_e32 vcc, s63, v133
	v_cmp_eq_u32_e64 s[2:3], s63, v133
	s_and_b64 s[44:45], vcc, s[38:39]
	s_and_b64 s[38:39], s[2:3], s[38:39]
	v_mbcnt_lo_u32_b32 v135, s44, 0
	v_mbcnt_hi_u32_b32 v135, s45, v135
	v_add_u32_e32 v135, s64, v135
	v_mad_i32_i24 v135, v135, v138, v139
	v_lshl_add_u32 v135, v135, 1, v140
	s_and_saveexec_b64 s[2:3], s[44:45]
	ds_write_b16 v135, v127
	s_mov_b64 exec, s[2:3]
	s_bcnt1_i32_b64 s60, s[44:45]
	s_add_i32 s64, s64, s60
	v_cmp_lt_u32_e32 vcc, s63, v134
	v_cmp_eq_u32_e64 s[2:3], s63, v134
	s_and_b64 s[44:45], vcc, s[40:41]
	s_and_b64 s[40:41], s[2:3], s[40:41]
	v_mbcnt_lo_u32_b32 v135, s44, 0
	v_mbcnt_hi_u32_b32 v135, s45, v135
	v_add_u32_e32 v135, s64, v135
	v_mad_i32_i24 v135, v135, v138, v139
	v_lshl_add_u32 v135, v135, 1, v140
	s_and_saveexec_b64 s[2:3], s[44:45]
	ds_write_b16 v135, v128
	s_mov_b64 exec, s[2:3]
	s_bcnt1_i32_b64 s60, s[44:45]
	s_add_i32 s64, s64, s60
	s_or_b64 s[44:45], s[42:43], s[36:37]
	s_or_b64 s[2:3], s[38:39], s[40:41]
	s_or_b64 s[44:45], s[44:45], s[2:3]
	s_cmp_eq_u64 s[44:45], 0
	s_cbranch_scc1 .Lrk_noapp
	v_add_u32_e32 v136, 0x400, v166
	v_mov_b32_e32 v137, 1
	s_mov_b64 s[2:3], exec
	s_and_b64 exec, s[2:3], s[42:43]
	ds_add_rtn_u32 v131, v136, v137
	s_and_b64 exec, s[2:3], s[36:37]
	ds_add_rtn_u32 v132, v136, v137
	s_and_b64 exec, s[2:3], s[38:39]
	ds_add_rtn_u32 v133, v136, v137
	s_and_b64 exec, s[2:3], s[40:41]
	ds_add_rtn_u32 v134, v136, v137
	s_mov_b64 exec, s[2:3]
	s_waitcnt lgkmcnt(0)
	v_lshl_add_u32 v131, v131, 2, v166
	v_lshl_add_u32 v132, v132, 2, v166
	v_lshl_add_u32 v133, v133, 2, v166
	v_lshl_add_u32 v134, v134, 2, v166
	s_and_b64 exec, s[2:3], s[42:43]
	ds_write_b32 v131, v129 offset:2048
	s_and_b64 exec, s[2:3], s[36:37]
	ds_write_b32 v132, v130 offset:2048
	s_and_b64 exec, s[2:3], s[38:39]
	ds_write_b32 v133, v5 offset:2048
	s_and_b64 exec, s[2:3], s[40:41]
	ds_write_b32 v134, v120 offset:2048
	s_mov_b64 exec, s[2:3]
.Lrk_noapp:
	s_waitcnt lgkmcnt(0)
	s_barrier
	s_and_saveexec_b64 s[2:3], s[44:45]
	s_cbranch_execz .Lrk_done
	v_mov_b32_e32 v131, 0
	v_mov_b32_e32 v132, 0
	v_mov_b32_e32 v133, 0
	v_mov_b32_e32 v134, 0
	v_add_u32_e32 v135, 0x800, v166
	s_mov_b32 s60, 0
.Lrk_tl:
	ds_read_b32 v136, v135
	v_add_u32_e32 v135, 4, v135
	s_add_i32 s60, s60, 1
	s_waitcnt lgkmcnt(0)
	v_cmp_gt_u32_e32 vcc, v136, v129
	v_cmp_gt_u32_e64 s[64:65], v136, v130
	s_nop 0
	v_addc_co_u32_e32 v131, vcc, 0, v131, vcc
	v_addc_co_u32_e64 v132, s[64:65], 0, v132, s[64:65]
	v_cmp_gt_u32_e32 vcc, v136, v5
	v_cmp_gt_u32_e64 s[64:65], v136, v120
	s_nop 0
	v_addc_co_u32_e32 v133, vcc, 0, v133, vcc
	v_addc_co_u32_e64 v134, s[64:65], 0, v134, s[64:65]
	s_cmp_lt_u32 s60, s62
	s_cbranch_scc1 .Lrk_tl
	v_subrev_u32_e32 v142, s61, v123
	v_add_u32_e32 v135, s61, v131
	v_add_u32_e32 v136, s61, v132
	v_add_u32_e32 v137, s61, v133
	v_add_u32_e32 v138, s61, v134
	v_lshl_add_u32 v135, v135, 1, v140
	v_lshl_add_u32 v136, v136, 1, v140
	v_lshl_add_u32 v137, v137, 1, v140
	v_lshl_add_u32 v138, v138, 1, v140
	v_cmp_gt_i32_e32 vcc, v142, v131
	v_cmp_gt_i32_e64 s[64:65], v142, v132
	s_and_b64 s[42:43], vcc, s[42:43]
	s_and_b64 s[36:37], s[64:65], s[36:37]
	v_cmp_gt_i32_e32 vcc, v142, v133
	v_cmp_gt_i32_e64 s[64:65], v142, v134
	s_and_b64 s[38:39], vcc, s[38:39]
	s_and_b64 s[40:41], s[64:65], s[40:41]
	s_mov_b64 exec, s[42:43]
	ds_write_b16 v135, v122
	s_mov_b64 exec, s[36:37]
	ds_write_b16 v136, v126
	s_mov_b64 exec, s[38:39]
	ds_write_b16 v137, v127
	s_mov_b64 exec, s[40:41]
	ds_write_b16 v138, v128
.Lrk_done:
	s_mov_b64 exec, s[2:3]
	s_and_saveexec_b64 s[2:3], s[4:5]
	ds_write_b32 v165, v231 offset:32
	s_or_b64 exec, exec, s[2:3]
